# speedup vs baseline: 1.0135x; 1.0135x over previous
_Z7k_fine3PKfS0_PKtS2_PKdS4_S0_PiPfS5_S0_S0_PtS7_:
	s_load_dwordx2 s[4:5], s[0:1], 0x30
	s_load_dwordx8 s[68:75], s[0:1], 0x0
	s_load_dwordx2 s[88:89], s[0:1], 0x48
	s_load_dwordx4 s[80:83], s[0:1], 0x20
	s_load_dwordx8 s[60:67], s[0:1], 0x50
	s_lshl_b32 s3, s2, 5
	s_and_b32 s3, s3, 0xe0
	s_lshr_b32 s76, s2, 3
	s_add_i32 s3, s3, s76
	s_lshr_b32 s84, s3, 1
	s_mov_b32 s85, 0
	s_lshl_b64 s[6:7], s[84:85], 14
	s_waitcnt lgkmcnt(0)
	s_add_u32 s4, s4, s6
	s_addc_u32 s5, s5, s7
	v_lshlrev_b32_e32 v2, 2, v0
	v_mov_b32_e32 v3, 0
	v_lshl_add_u64 v[4:5], s[4:5], 0, v[2:3]
	s_mov_b32 s6, 0x200000
	v_add_co_u32_e32 v6, vcc, s6, v4
	s_mov_b32 s7, 0x400000
	s_nop 0
	v_addc_co_u32_e32 v7, vcc, 0, v5, vcc
	v_or_b32_e32 v117, 0x400, v0
	v_add_co_u32_e32 v8, vcc, s7, v4
	v_lshlrev_b32_e32 v10, 2, v117
	v_mov_b32_e32 v11, v3
	v_addc_co_u32_e32 v9, vcc, 0, v5, vcc
	v_lshl_add_u64 v[12:13], s[4:5], 0, v[10:11]
	v_add_co_u32_e32 v14, vcc, s6, v12
	s_movk_i32 s8, 0x1000
	s_nop 0
	v_addc_co_u32_e32 v15, vcc, 0, v13, vcc
	v_add_co_u32_e32 v12, vcc, s7, v12
	v_or_b32_e32 v118, 0x800, v0
	s_nop 0
	v_addc_co_u32_e32 v13, vcc, 0, v13, vcc
	v_add_co_u32_e32 v16, vcc, s8, v4
	s_mov_b32 s8, 0x201000
	s_nop 0
	v_addc_co_u32_e32 v17, vcc, 0, v5, vcc
	v_add_co_u32_e32 v18, vcc, s8, v4
	s_mov_b32 s8, 0x401000
	s_nop 0
	v_addc_co_u32_e32 v19, vcc, 0, v5, vcc
	global_load_dword v24, v[6:7], off nt
	global_load_dword v25, v[8:9], off nt
	global_load_dword v26, v[8:9], off offset:2048 nt
	global_load_dword v27, v[14:15], off nt
	global_load_dword v28, v[12:13], off nt
	global_load_dword v29, v[16:17], off offset:2048 nt
	global_load_dword v30, v[18:19], off offset:2048 nt
	global_load_dword v31, v[6:7], off offset:2048 nt
	v_add_co_u32_e32 v6, vcc, s8, v4
	v_lshlrev_b32_e32 v8, 2, v118
	v_mov_b32_e32 v9, v3
	v_addc_co_u32_e32 v7, vcc, 0, v5, vcc
	v_lshl_add_u64 v[12:13], s[4:5], 0, v[8:9]
	global_load_dword v32, v2, s[4:5] nt
	global_load_dword v33, v2, s[4:5] offset:2048 nt
	global_load_dword v34, v10, s[4:5] nt
	global_load_dword v35, v8, s[4:5] nt
	v_add_co_u32_e32 v8, vcc, s6, v12
	s_movk_i32 s8, 0x2000
	s_nop 0
	v_addc_co_u32_e32 v9, vcc, 0, v13, vcc
	v_add_co_u32_e32 v10, vcc, s7, v12
	v_or_b32_e32 v1, 0xc00, v0
	s_nop 0
	v_addc_co_u32_e32 v11, vcc, 0, v13, vcc
	v_add_co_u32_e32 v12, vcc, s8, v4
	s_mov_b32 s8, 0x202000
	s_nop 0
	v_addc_co_u32_e32 v13, vcc, 0, v5, vcc
	v_add_co_u32_e32 v14, vcc, s8, v4
	s_mov_b32 s8, 0x402000
	s_nop 0
	v_addc_co_u32_e32 v15, vcc, 0, v5, vcc
	v_add_co_u32_e32 v16, vcc, s8, v4
	v_lshlrev_b32_e32 v18, 2, v1
	v_mov_b32_e32 v19, v3
	v_addc_co_u32_e32 v17, vcc, 0, v5, vcc
	v_lshl_add_u64 v[20:21], s[4:5], 0, v[18:19]
	v_add_co_u32_e32 v22, vcc, s6, v20
	s_movk_i32 s6, 0x3000
	s_nop 0
	v_addc_co_u32_e32 v23, vcc, 0, v21, vcc
	v_add_co_u32_e32 v20, vcc, s7, v20
	v_and_b32_e32 v124, 63, v0
	s_nop 0
	v_addc_co_u32_e32 v21, vcc, 0, v21, vcc
	global_load_dword v3, v[6:7], off offset:2048 nt
	global_load_dword v19, v[8:9], off nt
	global_load_dword v36, v[10:11], off nt
	global_load_dword v37, v[12:13], off offset:2048 nt
	global_load_dword v38, v[14:15], off offset:2048 nt
	global_load_dword v39, v[16:17], off offset:2048 nt
	global_load_dword v40, v[22:23], off nt
	global_load_dword v41, v[20:21], off nt
	v_add_co_u32_e32 v6, vcc, s6, v4
	s_mov_b32 s6, 0x203000
	s_nop 0
	v_addc_co_u32_e32 v7, vcc, 0, v5, vcc
	v_add_co_u32_e32 v8, vcc, s6, v4
	s_mov_b32 s6, 0x403000
	s_nop 0
	v_addc_co_u32_e32 v9, vcc, 0, v5, vcc
	v_add_co_u32_e32 v4, vcc, s6, v4
	v_lshrrev_b32_e32 v116, 6, v0
	s_nop 0
	v_addc_co_u32_e32 v5, vcc, 0, v5, vcc
	global_load_dword v13, v18, s[4:5] nt
	global_load_dword v14, v[6:7], off offset:2048 nt
	global_load_dword v15, v[8:9], off offset:2048 nt
	global_load_dword v16, v[4:5], off offset:2048 nt
	s_and_b32 s90, s84, 56
	s_lshl_b32 s91, s84, 3
	s_and_b32 s91, s91, 56
	s_or_b32 s90, s90, 4
	s_or_b32 s91, s91, 4
	s_lshr_b32 s92, s3, 7
	s_lshl_b32 s92, s92, 12
	v_lshrrev_b32_e32 v216, 5, v0
	v_mul_u32_u24_e32 v217, 57, v216
	v_lshrrev_b32_e32 v217, 9, v217
	v_mad_i32_i24 v216, v217, -9, v216
	v_add_u32_e32 v218, 1, v217
	v_mul_u32_u24_e32 v217, 0xab, v216
	v_lshrrev_b32_e32 v217, 9, v217
	v_mad_i32_i24 v216, v217, -3, v216
	v_add_u32_e32 v217, -1, v217
	v_add_u32_e32 v216, -1, v216
	v_mad_i32_i24 v217, v217, v218, s90
	v_mad_i32_i24 v216, v216, v218, s91
	v_lshl_add_u32 v217, v217, 6, v216
	v_add_u32_e32 v217, s92, v217
	v_and_b32_e32 v216, 31, v0
	v_lshlrev_b32_e32 v217, 9, v217
	v_lshl_add_u32 v217, v216, 4, v217
	global_load_dwordx4 v[220:223], v217, s[68:69]
	v_add_u32_e32 v219, 0x200, v0
	v_min_u32_e32 v219, 0x35f, v219
	v_lshrrev_b32_e32 v216, 5, v219
	v_mul_u32_u24_e32 v217, 57, v216
	v_lshrrev_b32_e32 v217, 9, v217
	v_mad_i32_i24 v216, v217, -9, v216
	v_add_u32_e32 v218, 1, v217
	v_mul_u32_u24_e32 v217, 0xab, v216
	v_lshrrev_b32_e32 v217, 9, v217
	v_mad_i32_i24 v216, v217, -3, v216
	v_add_u32_e32 v217, -1, v217
	v_add_u32_e32 v216, -1, v216
	v_mad_i32_i24 v217, v217, v218, s90
	v_mad_i32_i24 v216, v216, v218, s91
	v_lshl_add_u32 v217, v217, 6, v216
	v_add_u32_e32 v217, s92, v217
	v_and_b32_e32 v216, 31, v219
	v_lshlrev_b32_e32 v217, 9, v217
	v_lshl_add_u32 v217, v216, 4, v217
	global_load_dwordx4 v[224:227], v217, s[68:69]
	s_mov_b32 s4, 0xff800000
	v_cmp_eq_u32_e64 s[42:43], 0, v124
	s_waitcnt vmcnt(17)
	v_add_f32_e32 v4, v32, v24
	v_add_f32_e32 v12, v4, v25
	s_waitcnt vmcnt(16)
	v_add_f32_e32 v4, v33, v31
	s_waitcnt vmcnt(15)
	v_add_f32_e32 v5, v34, v27
	v_add_f32_e32 v11, v4, v26
	v_add_f32_e32 v10, v5, v28
	v_add_f32_e32 v5, v29, v30
	v_max3_f32 v4, v12, s4, v11
	s_waitcnt vmcnt(13)
	v_add_f32_e32 v9, v5, v3
	v_max3_f32 v3, v4, v10, v9
	s_waitcnt vmcnt(12)
	v_add_f32_e32 v4, v35, v19
	s_waitcnt vmcnt(11)
	v_add_f32_e32 v8, v4, v36
	s_waitcnt vmcnt(9)
	v_add_f32_e32 v4, v37, v38
	v_mbcnt_lo_u32_b32 v5, -1, 0
	s_waitcnt vmcnt(8)
	v_add_f32_e32 v7, v4, v39
	v_mbcnt_hi_u32_b32 v5, -1, v5
	v_max3_f32 v4, v3, v8, v7
	s_waitcnt vmcnt(5)
	v_add_f32_e32 v3, v13, v40
	v_and_b32_e32 v13, 64, v5
	v_add_f32_e32 v6, v3, v41
	s_waitcnt vmcnt(3)
	v_add_f32_e32 v3, v14, v15
	v_add_u32_e32 v13, 64, v13
	v_xor_b32_e32 v14, 1, v5
	v_cmp_lt_i32_e32 vcc, v14, v13
	s_waitcnt vmcnt(2)
	v_add_f32_e32 v3, v3, v16
	v_max3_f32 v4, v4, v6, v3
	v_cndmask_b32_e32 v14, v5, v14, vcc
	v_lshlrev_b32_e32 v115, 2, v14
	ds_bpermute_b32 v14, v115, v4
	s_waitcnt lgkmcnt(0)
	v_max_f32_e32 v14, v14, v14
	v_max_f32_e32 v4, v4, v14
	v_xor_b32_e32 v14, 2, v5
	v_cmp_lt_i32_e32 vcc, v14, v13
	s_nop 1
	v_cndmask_b32_e32 v14, v5, v14, vcc
	v_lshlrev_b32_e32 v114, 2, v14
	ds_bpermute_b32 v14, v114, v4
	s_waitcnt lgkmcnt(0)
	v_max_f32_e32 v14, v14, v14
	v_max_f32_e32 v4, v4, v14
	v_xor_b32_e32 v14, 4, v5
	v_cmp_lt_i32_e32 vcc, v14, v13
	s_nop 1
	v_cndmask_b32_e32 v14, v5, v14, vcc
	v_lshlrev_b32_e32 v113, 2, v14
	ds_bpermute_b32 v14, v113, v4
	s_waitcnt lgkmcnt(0)
	v_max_f32_e32 v14, v14, v14
	v_max_f32_e32 v4, v4, v14
	v_xor_b32_e32 v14, 8, v5
	v_cmp_lt_i32_e32 vcc, v14, v13
	s_nop 1
	v_cndmask_b32_e32 v14, v5, v14, vcc
	v_lshlrev_b32_e32 v112, 2, v14
	ds_bpermute_b32 v14, v112, v4
	s_waitcnt lgkmcnt(0)
	v_max_f32_e32 v14, v14, v14
	v_max_f32_e32 v4, v4, v14
	v_xor_b32_e32 v14, 16, v5
	v_cmp_lt_i32_e32 vcc, v14, v13
	s_nop 1
	v_cndmask_b32_e32 v14, v5, v14, vcc
	v_lshlrev_b32_e32 v122, 2, v14
	ds_bpermute_b32 v14, v122, v4
	s_waitcnt lgkmcnt(0)
	v_max_f32_e32 v14, v14, v14
	v_max_f32_e32 v4, v4, v14
	v_xor_b32_e32 v14, 32, v5
	v_cmp_lt_i32_e32 vcc, v14, v13
	s_nop 1
	v_cndmask_b32_e32 v5, v5, v14, vcc
	v_lshlrev_b32_e32 v121, 2, v5
	ds_bpermute_b32 v5, v121, v4
	s_and_saveexec_b64 s[4:5], s[42:43]
	s_cbranch_execz .LBB2_2
	s_waitcnt lgkmcnt(0)
	v_max_f32_e32 v5, v5, v5
	v_max_f32_e32 v4, v4, v4
	v_lshl_add_u32 v13, v116, 2, 0
	v_max_f32_e32 v4, v4, v5
	ds_write_b32 v13, v4 offset:65056
.LBB2_2:
	s_or_b64 exec, exec, s[4:5]
	v_cmp_eq_u32_e32 vcc, 0, v0
	s_and_saveexec_b64 s[4:5], vcc
	v_mov_b32_e32 v4, 0
	ds_write_b32 v4, v4 offset:65088
	s_or_b64 exec, exec, s[4:5]
	s_lshl_b32 s4, s84, 3
	s_and_b32 s77, s84, 56
	s_and_b32 s33, s4, 56
	s_movk_i32 s4, 0x360
	s_lshr_b32 s86, s3, 7
	s_or_b32 s10, s77, 4
	s_or_b32 s11, s33, 4
	s_mov_b32 s87, 0
	s_lshl_b64 s[6:7], s[86:87], 12
	s_mov_b64 s[8:9], 0
	s_movk_i32 s12, 0xab
	s_movk_i32 s13, 0x15f
	v_lshlrev_b32_e32 v228, 4, v0
	s_waitcnt vmcnt(1) lgkmcnt(0)
	ds_write_b128 v228, v[220:223]
	s_movk_i32 s4, 0x160
	v_cmp_gt_u32_e32 vcc, s4, v0
	s_and_saveexec_b64 s[4:5], vcc
	s_waitcnt vmcnt(0)
	ds_write_b128 v228, v[224:227] offset:8192
	s_or_b64 exec, exec, s[4:5]
	s_load_dwordx4 s[4:7], s[0:1], 0x38
	v_subrev_u32_e32 v2, 64, v0
	v_cmp_gt_u32_e32 vcc, 3, v2
	v_lshl_add_u32 v119, v0, 3, 0
	s_waitcnt lgkmcnt(0)
	v_writelane_b32 v212, s4, 0
	s_nop 1
	v_writelane_b32 v212, s5, 1
	v_writelane_b32 v212, s6, 2
	v_writelane_b32 v212, s7, 3
	s_and_saveexec_b64 s[0:1], vcc
	s_cbranch_execz .LBB2_9
	s_lshl_b32 s4, s86, 12
	s_or_b32 s6, s11, s4
	v_sub_u32_e32 v5, 63, v0
	v_add_lshl_u32 v4, s10, v5, 6
	v_add_u32_e32 v13, s6, v5
	v_or_b32_e32 v14, v13, v4
	v_mov_b32_e32 v15, 0
	s_or_b32 s7, s33, s4
	v_subrev_u32_e32 v2, 63, v0
	v_lshl_add_u64 v[16:17], v[14:15], 3, s[80:81]
	v_add_u32_e32 v14, s7, v4
	v_mov_b32_e32 v5, v15
	v_lshl_add_u64 v[18:19], v[14:15], 3, s[80:81]
	v_add_u32_e32 v14, s7, v2
	s_lshl_b32 s4, s10, 6
	v_lshl_add_u64 v[4:5], v[14:15], 0, v[4:5]
	v_or_b32_e32 v20, s4, v13
	v_mov_b32_e32 v21, v15
	s_mov_b32 s5, 0
	v_lshl_add_u64 v[4:5], v[4:5], 3, s[80:81]
	v_lshl_add_u64 v[20:21], v[20:21], 3, s[80:81]
	global_load_dwordx2 v[22:23], v[16:17], off
	global_load_dwordx2 v[24:25], v[18:19], off offset:32
	global_load_dwordx2 v[26:27], v[4:5], off offset:32
	global_load_dwordx2 v[28:29], v[20:21], off
	v_add_lshl_u32 v16, s10, v2, 6
	v_lshl_add_u64 v[4:5], v[14:15], 0, s[4:5]
	v_add_u32_e32 v14, v13, v16
	v_add_u32_e32 v16, s6, v16
	v_lshl_add_u64 v[4:5], v[4:5], 3, s[80:81]
	v_ashrrev_i32_e32 v15, 31, v14
	v_ashrrev_i32_e32 v17, 31, v16
	v_lshl_add_u64 v[14:15], v[14:15], 3, s[80:81]
	v_lshl_add_u64 v[18:19], v[16:17], 3, s[80:81]
	global_load_dwordx2 v[20:21], v[4:5], off offset:32
	global_load_dwordx2 v[30:31], v[14:15], off
	global_load_dwordx2 v[32:33], v[18:19], off
	v_add_u32_e32 v4, v16, v2
	v_ashrrev_i32_e32 v5, 31, v4
	v_lshl_add_u64 v[4:5], v[4:5], 3, s[80:81]
	global_load_dwordx2 v[4:5], v[4:5], off
	s_or_b32 s4, s7, s4
	s_lshl_b64 s[4:5], s[4:5], 3
	s_add_u32 s4, s80, s4
	s_addc_u32 s5, s81, s5
	s_load_dwordx2 s[4:5], s[4:5], 0x20
	s_mov_b32 s6, 0
	s_brev_b32 s7, 8
	v_mov_b32_e32 v2, 0x100
	v_mov_b32_e32 v13, 0xffffff80
	v_mov_b32_e32 v34, 0x260
	s_waitcnt vmcnt(7)
	v_add_f64 v[14:15], v[22:23], 0
	s_waitcnt vmcnt(6)
	v_add_f64 v[14:15], v[14:15], v[24:25]
	s_waitcnt vmcnt(5)
	v_add_f64 v[14:15], v[14:15], v[26:27]
	s_waitcnt vmcnt(4)
	v_add_f64 v[14:15], v[14:15], v[28:29]
	s_waitcnt lgkmcnt(0)
	v_add_f64 v[14:15], v[14:15], s[4:5]
	s_mov_b32 s4, 0x812dea11
	s_mov_b32 s5, 0x3d719799
	s_waitcnt vmcnt(3)
	v_add_f64 v[14:15], v[14:15], v[20:21]
	s_waitcnt vmcnt(2)
	v_add_f64 v[14:15], v[14:15], v[30:31]
	s_waitcnt vmcnt(1)
	v_add_f64 v[14:15], v[14:15], v[32:33]
	s_waitcnt vmcnt(0)
	v_add_f64 v[4:5], v[14:15], v[4:5]
	v_cmp_gt_f64_e32 vcc, s[6:7], v[4:5]
	s_nop 1
	v_cndmask_b32_e32 v2, 0, v2, vcc
	v_ldexp_f64 v[4:5], v[4:5], v2
	v_rsq_f64_e32 v[14:15], v[4:5]
	v_cndmask_b32_e32 v2, 0, v13, vcc
	v_cmp_class_f64_e32 vcc, v[4:5], v34
	v_mul_f64 v[16:17], v[4:5], v[14:15]
	v_mul_f64 v[14:15], v[14:15], 0.5
	v_fma_f64 v[18:19], -v[14:15], v[16:17], 0.5
	v_fmac_f64_e32 v[16:17], v[16:17], v[18:19]
	v_fmac_f64_e32 v[14:15], v[14:15], v[18:19]
	v_fma_f64 v[18:19], -v[16:17], v[16:17], v[4:5]
	v_fmac_f64_e32 v[16:17], v[18:19], v[14:15]
	v_fma_f64 v[18:19], -v[16:17], v[16:17], v[4:5]
	v_fmac_f64_e32 v[16:17], v[18:19], v[14:15]
	v_ldexp_f64 v[14:15], v[16:17], v2
	v_cndmask_b32_e32 v5, v15, v5, vcc
	v_cndmask_b32_e32 v4, v14, v4, vcc
	v_max_f64 v[4:5], v[4:5], s[4:5]
	v_div_scale_f64 v[14:15], s[4:5], v[4:5], v[4:5], 1.0
	v_rcp_f64_e32 v[16:17], v[14:15]
	v_div_scale_f64 v[18:19], vcc, 1.0, v[4:5], 1.0
	v_fma_f64 v[20:21], -v[14:15], v[16:17], 1.0
	v_fmac_f64_e32 v[16:17], v[16:17], v[20:21]
	v_fma_f64 v[20:21], -v[14:15], v[16:17], 1.0
	v_fmac_f64_e32 v[16:17], v[16:17], v[20:21]
	v_mul_f64 v[20:21], v[18:19], v[16:17]
	v_fma_f64 v[14:15], -v[14:15], v[20:21], v[18:19]
	v_div_fmas_f64 v[14:15], v[14:15], v[16:17], v[20:21]
	v_div_fixup_f64 v[4:5], v[14:15], v[4:5], 1.0
	ds_write_b64 v119, v[4:5] offset:64512

	.amdhsa_kernel _Z7k_fine3PKfS0_PKtS2_PKdS4_S0_PiPfS5_S0_S0_PtS7_
		.amdhsa_group_segment_fixed_size 0
		.amdhsa_private_segment_fixed_size 0
		.amdhsa_kernarg_size 112
		.amdhsa_user_sgpr_count 2
		.amdhsa_user_sgpr_dispatch_ptr 0
		.amdhsa_user_sgpr_queue_ptr 0
		.amdhsa_user_sgpr_kernarg_segment_ptr 1
		.amdhsa_user_sgpr_dispatch_id 0
		.amdhsa_user_sgpr_kernarg_preload_length 0
		.amdhsa_user_sgpr_kernarg_preload_offset 0
		.amdhsa_user_sgpr_private_segment_size 0
		.amdhsa_uses_dynamic_stack 0
		.amdhsa_enable_private_segment 0
		.amdhsa_system_sgpr_workgroup_id_x 1
		.amdhsa_system_sgpr_workgroup_id_y 0
		.amdhsa_system_sgpr_workgroup_id_z 0
		.amdhsa_system_sgpr_workgroup_info 0
		.amdhsa_system_vgpr_workitem_id 0
		.amdhsa_next_free_vgpr 229
		.amdhsa_next_free_sgpr 100
		.amdhsa_accum_offset 232
		.amdhsa_reserve_vcc 1
		.amdhsa_float_round_mode_32 0
		.amdhsa_float_round_mode_16_64 0
		.amdhsa_float_denorm_mode_32 3
		.amdhsa_float_denorm_mode_16_64 3
		.amdhsa_dx10_clamp 1
		.amdhsa_ieee_mode 1
		.amdhsa_fp16_overflow 0
		.amdhsa_tg_split 0
		.amdhsa_exception_fp_ieee_invalid_op 0
		.amdhsa_exception_fp_denorm_src 0
		.amdhsa_exception_fp_ieee_div_zero 0
		.amdhsa_exception_fp_ieee_overflow 0
		.amdhsa_exception_fp_ieee_underflow 0
		.amdhsa_exception_fp_ieee_inexact 0
		.amdhsa_exception_int_div_zero 0
	.end_amdhsa_kernel

amdhsa.kernels:
  - .agpr_count:     0
    .args:
      - .actual_access:  read_only
        .address_space:  global
        .offset:         0
        .size:           8
        .value_kind:     global_buffer
      - .actual_access:  read_only
        .address_space:  global
        .offset:         8
        .size:           8
        .value_kind:     global_buffer
      - .actual_access:  write_only
        .address_space:  global
        .offset:         16
        .size:           8
        .value_kind:     global_buffer
      - .actual_access:  write_only
        .address_space:  global
        .offset:         24
        .size:           8
        .value_kind:     global_buffer
      - .actual_access:  write_only
        .address_space:  global
        .offset:         32
        .size:           8
        .value_kind:     global_buffer
      - .actual_access:  write_only
        .address_space:  global
        .offset:         40
        .size:           8
        .value_kind:     global_buffer
      - .actual_access:  write_only
        .address_space:  global
        .offset:         48
        .size:           8
        .value_kind:     global_buffer
      - .actual_access:  write_only
        .address_space:  global
        .offset:         56
        .size:           8
        .value_kind:     global_buffer
      - .actual_access:  write_only
        .address_space:  global
        .offset:         64
        .size:           8
        .value_kind:     global_buffer
    .group_segment_fixed_size: 18944
    .kernarg_segment_align: 8
    .kernarg_segment_size: 72
    .language:       OpenCL C
    .language_version:
      - 2
      - 0
    .max_flat_workgroup_size: 256
    .name:           _Z6k_prepPKfS0_PfS1_PdS2_PtS3_S3_
    .private_segment_fixed_size: 0
    .sgpr_count:     34
    .sgpr_spill_count: 0
    .symbol:         _Z6k_prepPKfS0_PfS1_PdS2_PtS3_S3_.kd
    .uniform_work_group_size: 1
    .uses_dynamic_stack: false
    .vgpr_count:     29
    .vgpr_spill_count: 0
    .wavefront_size: 64
  - .agpr_count:     16
    .args:
      - .actual_access:  read_only
        .address_space:  global
        .offset:         0
        .size:           8
        .value_kind:     global_buffer
      - .actual_access:  read_only
        .address_space:  global
        .offset:         8
        .size:           8
        .value_kind:     global_buffer
      - .actual_access:  read_only
        .address_space:  global
        .offset:         16
        .size:           8
        .value_kind:     global_buffer
      - .actual_access:  read_only
        .address_space:  global
        .offset:         24
        .size:           8
        .value_kind:     global_buffer
      - .actual_access:  write_only
        .address_space:  global
        .offset:         32
        .size:           8
        .value_kind:     global_buffer
    .group_segment_fixed_size: 256
    .kernarg_segment_align: 8
    .kernarg_segment_size: 40
    .language:       OpenCL C
    .language_version:
      - 2
      - 0
    .max_flat_workgroup_size: 256
    .name:           _Z9k_coarse2PKtS0_PKdS2_Pf
    .private_segment_fixed_size: 0
    .sgpr_count:     37
    .sgpr_spill_count: 0
    .symbol:         _Z9k_coarse2PKtS0_PKdS2_Pf.kd
    .uniform_work_group_size: 1
    .uses_dynamic_stack: false
    .vgpr_count:     132
    .vgpr_spill_count: 0
    .wavefront_size: 64
  - .agpr_count:     0
    .args:
      - .actual_access:  read_only
        .address_space:  global
        .offset:         0
        .size:           8
        .value_kind:     global_buffer
      - .actual_access:  read_only
        .address_space:  global
        .offset:         8
        .size:           8
        .value_kind:     global_buffer
      - .actual_access:  read_only
        .address_space:  global
        .offset:         16
        .size:           8
        .value_kind:     global_buffer
      - .actual_access:  read_only
        .address_space:  global
        .offset:         24
        .size:           8
        .value_kind:     global_buffer
      - .actual_access:  read_only
        .address_space:  global
        .offset:         32
        .size:           8
        .value_kind:     global_buffer
      - .actual_access:  read_only
        .address_space:  global
        .offset:         40
        .size:           8
        .value_kind:     global_buffer
      - .actual_access:  read_only
        .address_space:  global
        .offset:         48
        .size:           8
        .value_kind:     global_buffer
      - .actual_access:  write_only
        .address_space:  global
        .offset:         56
        .size:           8
        .value_kind:     global_buffer
      - .actual_access:  write_only
        .address_space:  global
        .offset:         64
        .size:           8
        .value_kind:     global_buffer
      - .actual_access:  write_only
        .address_space:  global
        .offset:         72
        .size:           8
        .value_kind:     global_buffer
      - .actual_access:  read_only
        .address_space:  global
        .offset:         80
        .size:           8
        .value_kind:     global_buffer
      - .actual_access:  read_only
        .address_space:  global
        .offset:         88
        .size:           8
        .value_kind:     global_buffer
      - .actual_access:  write_only
        .address_space:  global
        .offset:         96
        .size:           8
        .value_kind:     global_buffer
      - .actual_access:  write_only
        .address_space:  global
        .offset:         104
        .size:           8
        .value_kind:     global_buffer
    .group_segment_fixed_size: 0
    .kernarg_segment_align: 8
    .kernarg_segment_size: 112
    .language:       OpenCL C
    .language_version:
      - 2
      - 0
    .max_flat_workgroup_size: 512
    .name:           _Z7k_fine3PKfS0_PKtS2_PKdS4_S0_PiPfS5_S0_S0_PtS7_
    .private_segment_fixed_size: 0
    .sgpr_count:     106
    .sgpr_spill_count: 4
    .symbol:         _Z7k_fine3PKfS0_PKtS2_PKdS4_S0_PiPfS5_S0_S0_PtS7_.kd
    .uniform_work_group_size: 1
    .uses_dynamic_stack: false
    .vgpr_count:     229
    .vgpr_spill_count: 0
    .wavefront_size: 64
  - .agpr_count:     0
    .args:
      - .actual_access:  read_only
        .address_space:  global
        .offset:         0
        .size:           8
        .value_kind:     global_buffer
      - .actual_access:  read_only
        .address_space:  global
        .offset:         8
        .size:           8
        .value_kind:     global_buffer
      - .actual_access:  read_only
        .address_space:  global
        .offset:         16
        .size:           8
        .value_kind:     global_buffer
      - .actual_access:  read_only
        .address_space:  global
        .offset:         24
        .size:           8
        .value_kind:     global_buffer
      - .actual_access:  read_only
        .address_space:  global
        .offset:         32
        .size:           8
        .value_kind:     global_buffer
      - .actual_access:  read_only
        .address_space:  global
        .offset:         40
        .size:           8
        .value_kind:     global_buffer
      - .actual_access:  write_only
        .address_space:  global
        .offset:         48
        .size:           8
        .value_kind:     global_buffer
      - .actual_access:  write_only
        .address_space:  global
        .offset:         56
        .size:           8
        .value_kind:     global_buffer
      - .actual_access:  write_only
        .address_space:  global
        .offset:         64
        .size:           8
        .value_kind:     global_buffer
    .group_segment_fixed_size: 18512
    .kernarg_segment_align: 8
    .kernarg_segment_size: 72
    .language:       OpenCL C
    .language_version:
      - 2
      - 0
    .max_flat_workgroup_size: 256
    .name:           _Z10k_transferPKtS0_PKfPKiS2_S4_PfS5_S5_
    .private_segment_fixed_size: 0
    .sgpr_count:     34
    .sgpr_spill_count: 0
    .symbol:         _Z10k_transferPKtS0_PKfPKiS2_S4_PfS5_S5_.kd
    .uniform_work_group_size: 1
    .uses_dynamic_stack: false
    .vgpr_count:     49
    .vgpr_spill_count: 0
    .wavefront_size: 64
